# layer-1 expert weight conversion: first part (6 items per wave) runs at the end of the layer-0 MoE phase on workgroups that finish it early (vcu >= 3*nl); phase 9 converts the rest
# speedup vs baseline: 1.0081x; 1.0081x over previous
.LBB0_1151:
	v_mov_b32_e32 v1, 0x224f0
	ds_read_b32 v1, v1
	s_waitcnt lgkmcnt(0)
	v_readfirstlane_b32 s0, v1
	s_lshl_b32 s0, s0, 2
	s_sub_i32 s0, s0, s33
	s_max_i32 s0, s0, 0
	s_mul_i32 s0, s0, 3
	s_sub_i32 s1, s33, s0
	s_cmp_lt_i32 s1, 1
	s_cbranch_scc1 .Lcv_skip
	s_cmp_lt_i32 s95, s0
	s_cbranch_scc1 .Lcv_skip
	s_lshl_b32 s12, s1, 3
	s_mul_i32 s13, s1, 48
	s_min_i32 s13, s13, 0x1800
	s_sub_i32 s14, s95, s0
	s_lshl_b32 s14, s14, 3
	s_add_i32 s34, s14, s92
	s_addk_i32 s12, 0x200
	s_cmp_ge_i32 s34, s13
	s_cbranch_scc1 .Lcv_skip
	s_mov_b64 s[4:5], -1
	s_cmp_lt_i32 s34, s13
	s_cselect_b64 s[6:7], -1, 0
	s_and_b64 s[8:9], s[6:7], exec
	s_cselect_b32 s16, s34, 0
	s_cmpk_gt_i32 s16, 0xfff
	s_cbranch_scc0 .Lcv1379
	s_bfe_u32 s8, s16, 0x20007
	s_cmp_lt_i32 s8, 1
	s_mov_b32 s17, 4
	s_cbranch_scc1 .Lcv1384
	s_cmp_eq_u32 s8, 1
	s_cbranch_scc1 .Lcv1381
	s_cmp_eq_u32 s8, 2
	s_cselect_b32 s17, 5, 7
	s_mov_b64 s[4:5], 0
	s_branch .Lcv1382

.Lcv1403:
.Lcv1404:
	s_and_b64 vcc, exec, s[4:5]
	s_cbranch_vccnz .Lcv_done
	s_mul_hi_i32 s5, s16, s35
	s_mul_i32 s4, s16, s35
	s_lshl_b64 s[4:5], s[4:5], 1
	s_add_u32 s4, s10, s4
	s_addc_u32 s5, s11, s5
	s_lshl_b32 s6, s9, 1
	s_add_u32 s10, s4, s6
	s_mul_i32 s4, s92, 0x2200
	v_lshrrev_b32_e32 v82, 3, v208
	v_and_b32_e32 v36, 56, v158
	s_addc_u32 s11, s5, 0
	s_add_i32 s4, s4, 0
	v_mul_u32_u24_e32 v1, 0x84, v36
	v_or_b32_e32 v84, 8, v82
	v_lshlrev_b32_e32 v38, 2, v82
	v_lshl_add_u32 v35, v34, 2, s4
	v_mul_u32_u24_e32 v37, 0x84, v82
	v_add3_u32 v1, s4, v1, v38
	v_mul_u32_u24_e32 v38, 0x84, v84
	s_mov_b32 s7, 0
	s_add_i32 s36, s12, 0xfffffe00
	v_mov_b32_e32 v81, 0
	v_or_b32_e32 v88, 16, v82
	v_or_b32_e32 v90, 24, v82
	v_lshlrev_b32_e32 v92, 2, v34
	v_add_u32_e32 v67, v35, v37
	v_add_u32_e32 v69, v35, v38
	v_lshlrev_b32_e32 v94, 1, v36
	s_branch .Lcv1407
.Lcv1406:
	s_mul_hi_i32 s5, s18, s38
	s_mul_i32 s4, s18, s38
	s_lshl_b64 s[4:5], s[4:5], 1
	s_add_u32 s4, s16, s4
	s_addc_u32 s5, s17, s5
	s_lshl_b32 s6, s39, 1
	s_waitcnt lgkmcnt(0)
	s_add_u32 s10, s4, s6
	s_addc_u32 s11, s5, 0
	s_add_i32 s34, s34, s36
	v_mov_b64_e32 v[30:31], v[62:63]
	s_cmp_lt_i32 s34, s13
	v_mov_b64_e32 v[32:33], v[64:65]
	v_mov_b32_e32 v78, v87
	v_mov_b32_e32 v86, v85
	v_mov_b32_e32 v74, v83
	v_mov_b32_e32 v76, v79
	v_mov_b32_e32 v70, v77
	v_mov_b32_e32 v72, v75
	v_mov_b32_e32 v66, v73
	v_mov_b32_e32 v68, v71
	s_mov_b32 s8, s37
	s_mov_b32 s35, s38
	v_mov_b32_e32 v26, v58
	v_mov_b32_e32 v27, v59
	v_mov_b32_e32 v28, v60
	v_mov_b32_e32 v29, v61
	v_mov_b32_e32 v22, v54
	v_mov_b32_e32 v23, v55
	v_mov_b32_e32 v24, v56
	v_mov_b32_e32 v25, v57
	v_mov_b32_e32 v18, v50
	v_mov_b32_e32 v19, v51
	v_mov_b32_e32 v20, v52
	v_mov_b32_e32 v21, v53
	v_mov_b32_e32 v14, v46
	v_mov_b32_e32 v15, v47
	v_mov_b32_e32 v16, v48
	v_mov_b32_e32 v17, v49
	v_mov_b32_e32 v10, v42
	v_mov_b32_e32 v11, v43
	v_mov_b32_e32 v12, v44
	v_mov_b32_e32 v13, v45
	v_mov_b32_e32 v6, v38
	v_mov_b32_e32 v7, v39
	v_mov_b32_e32 v8, v40
	v_mov_b32_e32 v9, v41
	v_mov_b32_e32 v2, v34
	v_mov_b32_e32 v3, v35
	v_mov_b32_e32 v4, v36
	v_mov_b32_e32 v5, v37
	s_cbranch_scc0 .Lcv_done
.Lcv1407:
	s_add_i32 s4, s12, s34
	s_add_i32 s6, s4, 0xfffffe00
	s_cmp_ge_i32 s6, s13
	s_cselect_b64 s[4:5], -1, 0
	s_cmp_lt_i32 s6, s13
	s_cselect_b32 s9, s6, s34
	s_cmpk_gt_i32 s9, 0xfff
	s_mov_b64 s[18:19], -1
	s_cbranch_scc0 .Lcv1414
	s_bfe_u32 s18, s9, 0x20007
	s_cmp_lt_i32 s18, 1
	s_mov_b32 s19, 4
	s_cbranch_scc1 .Lcv1413
	s_cmp_eq_u32 s18, 1
	s_mov_b64 s[16:17], -1
	s_cbranch_scc1 .Lcv1411
	s_cmp_eq_u32 s18, 2
	s_cselect_b32 s19, 5, 7
	s_mov_b64 s[16:17], 0

.Lcv1441:
	ds_read2_b32 v[2:3], v10 offset0:24 offset1:57
	ds_read2_b32 v[4:5], v10 offset0:90 offset1:123
	ds_read2_b32 v[8:9], v10 offset0:156 offset1:189
	ds_read2_b32 v[10:11], v10 offset0:222 offset1:255
	s_and_b64 vcc, exec, s[4:5]
	s_waitcnt lgkmcnt(3)
	v_cvt_pk_bf16_f32 v2, v2, v3
	s_waitcnt lgkmcnt(2)
	v_cvt_pk_bf16_f32 v3, v4, v5
	s_waitcnt lgkmcnt(1)
	v_cvt_pk_bf16_f32 v4, v8, v9
	v_mad_u64_u32 v[8:9], s[10:11], s35, v90, 0
	s_waitcnt lgkmcnt(0)
	v_cvt_pk_bf16_f32 v5, v10, v11
	v_lshl_add_u64 v[6:7], v[8:9], 1, v[6:7]
	global_store_dwordx4 v[6:7], v[2:5], off sc1
	s_cbranch_vccnz .Lcv1406
	v_lshl_add_u64 v[6:7], s[8:9], 1, v[6:7]
	global_store_dwordx4 v[6:7], v[2:5], off sc1
	s_branch .Lcv1406
.Lcv_done:
	s_waitcnt lgkmcnt(0)
.Lcv_skip:
	s_cmp_gt_i32 s81, 7
	s_cselect_b64 s[4:5], -1, 0
	s_and_b64 s[0:1], s[76:77], s[4:5]
	v_readlane_b32 s86, v253, 40
	s_andn2_b64 vcc, exec, s[0:1]
	v_readlane_b32 s76, v253, 62
	v_readlane_b32 s77, v253, 63
	v_readlane_b32 s87, v253, 41
	s_cbranch_vccnz .LBB0_1205
	s_waitcnt vmcnt(0)
	s_waitcnt vmcnt(0) lgkmcnt(0)
	s_barrier
	s_and_saveexec_b64 s[0:1], s[78:79]
	s_cbranch_execz .LBB0_1204
	v_mov_b32_e32 v1, 0x22160
	s_waitcnt vmcnt(0) lgkmcnt(0)
	ds_read_b32 v2, v1
	v_mov_b32_e32 v3, 1
	v_mov_b32_e32 v4, s99
	v_and_b32_e32 v5, 0xffff, v4
	v_lshrrev_b32_e32 v6, 16, v4
	global_atomic_add v7, v5, v3, s[100:101] sc0
	buffer_inv sc1
	v_lshrrev_b32_e32 v8, 8, v5
	v_sub_u32_e32 v8, s98, v8
	v_add_u32_e32 v8, 7, v8
	v_lshrrev_b32_e32 v8, 3, v8
	v_mov_b32_e32 v9, s98
	v_min_u32_e32 v9, 8, v9
	v_mov_b32_e32 v10, 0
	s_waitcnt lgkmcnt(0)
	v_add_u32_e32 v2, 1, v2
	ds_write_b32 v1, v2
	v_mul_lo_u32 v8, v8, v2
	v_mul_lo_u32 v9, v9, v2
	s_waitcnt vmcnt(0)
	v_add_u32_e32 v7, 1, v7
	v_cmp_eq_u32_e32 vcc, v7, v8
	s_cbranch_vccz .Lgb_poll_7
	v_mov_b32_e32 v4, 0
	global_atomic_add v4, v3, s[100:101] offset:2048
	global_atomic_add v4, v3, s[100:101] offset:2304
	global_atomic_add v4, v3, s[100:101] offset:2560
	global_atomic_add v4, v3, s[100:101] offset:2816
	global_atomic_add v4, v3, s[100:101] offset:3072
	global_atomic_add v4, v3, s[100:101] offset:3328
	global_atomic_add v4, v3, s[100:101] offset:3584
	global_atomic_add v4, v3, s[100:101] offset:3840

.LBB0_1374:
	s_cmp_lt_i32 s89, 32
	s_cselect_b64 s[6:7], -1, 0
	s_xor_b64 s[8:9], s[16:17], -1
	s_or_b64 s[6:7], s[6:7], s[8:9]
	s_mov_b64 s[4:5], -1
	s_and_b64 vcc, exec, s[6:7]
	s_cbranch_vccnz .LBB0_1443
	s_lshl_b32 s6, s89, 3
	s_add_i32 s6, s6, s92
	s_add_i32 s34, s6, 0xffffff00
	v_mov_b32_e32 v1, 0x224f0
	ds_read_b32 v1, v1
	s_waitcnt lgkmcnt(0)
	v_readfirstlane_b32 s7, v1
	s_lshl_b32 s7, s7, 2
	s_sub_i32 s7, s7, s33
	s_max_i32 s7, s7, 0
	s_mul_i32 s7, s7, 3
	s_sub_i32 s7, s33, s7
	s_max_i32 s7, s7, 0
	s_mul_i32 s7, s7, 48
	s_min_i32 s7, s7, 0x1800
	s_add_i32 s34, s34, s7
	s_cmpk_lt_i32 s34, 0x1800
	s_cselect_b64 s[6:7], -1, 0
	s_and_b64 s[8:9], s[6:7], exec
	s_cselect_b32 s16, s34, 0
	s_cmpk_gt_i32 s16, 0xfff
	s_cbranch_scc0 .LBB0_1379
	s_bfe_u32 s8, s16, 0x20007
	s_cmp_lt_i32 s8, 1
	s_mov_b32 s17, 4
	s_cbranch_scc1 .LBB0_1384
	s_cmp_eq_u32 s8, 1
	s_cbranch_scc1 .LBB0_1381
	s_cmp_eq_u32 s8, 2
	s_cselect_b32 s17, 5, 7
	s_mov_b64 s[4:5], 0
	s_branch .LBB0_1382
